# code placement: 4-byte pads so the INPROJ bf16, MERGE, OUT and MoE gate/up K-loops sit at the baseline's 8-byte instruction phase again (on top of v34)
# baseline (speedup 1.0000x reference)
.LBB0_277:
	s_nop 0
	s_mul_i32 s0, s8, 10
	s_add_i32 s4, s0, 2
	s_cmp_lg_u32 s8, 0
	v_writelane_b32 v254, s0, 39
	s_cselect_b64 s[0:1], -1, 0
	v_writelane_b32 v254, s0, 40
	s_cmp_eq_u32 s8, 0
	v_readlane_b32 s6, v252, 6
	v_writelane_b32 v254, s1, 41
	s_mov_b32 s0, s8
	v_writelane_b32 v254, s0, 42
	v_readlane_b32 s7, v252, 7
	s_nop 0
	v_writelane_b32 v254, s1, 43
	s_cselect_b64 s[0:1], -1, 0
	v_writelane_b32 v254, s0, 44
	s_cmp_le_i32 s6, s4
	s_nop 0
	v_writelane_b32 v254, s1, 45
	s_cselect_b64 s[0:1], -1, 0
	s_cmp_lt_i32 s4, s7
	s_cselect_b64 s[4:5], -1, 0
	s_and_b64 s[74:75], s[0:1], s[4:5]
	s_andn2_b64 vcc, exec, s[74:75]
	s_cbranch_vccnz .LBB0_460
	v_readlane_b32 s0, v254, 40
	v_readlane_b32 s1, v254, 41
	s_and_b64 s[0:1], s[0:1], exec
	s_movk_i32 s0, 0x88
	s_cselect_b32 s83, 0x80, s0
	v_readlane_b32 s10, v252, 4
	s_mul_i32 s6, s83, 6
	v_readlane_b32 s0, v252, 0
	v_readlane_b32 s11, v252, 5
	s_cmp_lt_i32 s0, s6
	s_cselect_b64 s[28:29], -1, 0
	s_lshr_b32 s7, s6, 3
	s_waitcnt vmcnt(0)
	v_mbcnt_lo_u32_b32 v3, -1, 0
	v_mbcnt_hi_u32_b32 v3, -1, v3
	s_cmp_ge_i32 s0, s6
	v_add_u32_e32 v0, s15, v3
	s_nop 0
	v_readfirstlane_b32 s30, v0
	s_cbranch_scc1 .LBB0_280
	v_readlane_b32 s0, v252, 12
	s_or_b32 s0, s7, s0
	v_readlane_b32 s1, v253, 15
	s_mul_i32 s0, s0, s1
	v_readlane_b32 s1, v253, 16
	s_add_i32 s0, s0, s1
	s_mul_hi_i32 s1, s0, 0x2aaaaaab
	s_lshr_b32 s4, s1, 31
	s_ashr_i32 s1, s1, 2
	s_add_i32 s1, s1, s4
	s_lshl_b32 s5, s1, 2
	s_sub_i32 s4, s83, s5
	s_min_i32 s8, s4, 4
	s_sext_i32_i8 s4, s8
	v_cvt_f32_i32_e32 v2, s4
	s_mul_i32 s1, s1, 24
	s_sub_i32 s9, s0, s1
	v_cvt_f32_i32_e32 v4, s9
	v_rcp_iflag_f32_e32 v5, v2
	s_xor_b32 s0, s9, s4
	s_ashr_i32 s0, s0, 30
	s_or_b32 s4, s0, 1
	v_mul_f32_e32 v5, v4, v5
	v_trunc_f32_e32 v5, v5
	v_fma_f32 v4, -v5, v2, v4
	v_cvt_i32_f32_e32 v5, v5
	v_cmp_ge_f32_e64 s[0:1], |v4|, |v2|
	s_and_b64 s[0:1], s[0:1], exec
	s_cselect_b32 s0, s4, 0
	v_readfirstlane_b32 s1, v5
	s_add_i32 s0, s1, s0
	s_sext_i32_i8 s4, s0
	s_mul_i32 s0, s0, s8
	s_sub_i32 s0, s9, s0
	s_sext_i32_i8 s0, s0
	s_add_i32 s0, s5, s0

.LBB0_358:
	s_nop 0
	s_andn2_b64 vcc, exec, s[28:29]
	s_cbranch_vccnz .LBB0_284
	s_barrier
	s_branch .LBB0_284

.LBB0_1343:
	s_andn2_b64 vcc, exec, s[0:1]
	v_readlane_b32 s0, v252, 43
	v_readlane_b32 s1, v252, 44
	s_nop 1
	v_cndmask_b32_e64 v0, 0, 1, s[0:1]
	v_cmp_ne_u32_e64 s[38:39], 1, v0
	s_cbranch_vccnz .LBB0_1531
	s_nop 0
	v_readlane_b32 s6, v252, 4
	v_readlane_b32 s7, v252, 5
	s_waitcnt vmcnt(0)
	v_mbcnt_lo_u32_b32 v3, -1, 0
	v_mbcnt_hi_u32_b32 v3, -1, v3
	s_and_b64 vcc, exec, s[38:39]
	v_add_u32_e32 v0, s15, v3
	s_nop 0
	v_readfirstlane_b32 s0, v0
	s_cbranch_vccnz .LBB0_1347
	v_readlane_b32 s4, v252, 45
	v_readlane_b32 s8, v254, 40
	v_readlane_b32 s5, v252, 46
	v_readlane_b32 s9, v254, 41
	s_or_b64 s[4:5], s[4:5], s[8:9]
	s_and_b64 vcc, exec, s[4:5]
	s_cbranch_vccnz .LBB0_1348
	s_mov_b64 s[8:9], -1
	v_readlane_b32 s23, v252, 49
	s_branch .LBB0_1349

.LBB0_2062:
	s_andn2_b64 vcc, exec, s[0:1]
	s_cbranch_vccnz .LBB0_2145
	s_nop 0
	v_readlane_b32 s0, v252, 4
	v_readlane_b32 s4, v254, 7
	v_readlane_b32 s1, v252, 5
	s_waitcnt vmcnt(0)
	v_mbcnt_lo_u32_b32 v10, -1, 0
	v_mbcnt_hi_u32_b32 v10, -1, v10
	v_mov_b32_e32 v2, s4
	ds_read_b32 v2, v2
	v_add_u32_e32 v0, s15, v10
	s_waitcnt lgkmcnt(0)
	v_readfirstlane_b32 s4, v2
	s_ashr_i32 s5, s4, 31
	s_lshr_b32 s5, s5, 24
	s_add_i32 s4, s4, s5
	s_ashr_i32 s9, s4, 8
	v_readlane_b32 s4, v252, 57
	v_readlane_b32 s5, v252, 58
	v_readfirstlane_b32 s8, v0
	s_and_b64 vcc, exec, s[4:5]
	s_cbranch_vccz .LBB0_2065
	s_lshl_b32 s4, s9, 2
	v_readlane_b32 s5, v252, 0
	s_cmp_lt_i32 s5, s4
	s_mov_b64 s[6:7], 0
	s_cselect_b64 s[4:5], -1, 0
	s_branch .LBB0_2066
